# grid barrier: acquire-side cache invalidate issued right after arrival (overlapped with the wait) instead of after the release; leaders invalidate behind their top-level arrival
# speedup vs baseline: 1.0077x; 1.0075x over previous
; DI unsigned xb_ld(unsigned* p)              { return __hip_atomic_load(p, __ATOMIC_RELAXED, __HIP_MEMORY_SCOPE_AGENT); }
; DI unsigned xb_add(unsigned* p, unsigned v) { return __hip_atomic_fetch_add(p, v, __ATOMIC_RELAXED, __HIP_MEMORY_SCOPE_AGENT); }
; #define XB_SPIN(cond, bar) do { unsigned _sp = 0; while (cond) { __builtin_amdgcn_s_sleep(1); \
;     if ((++_sp & 255u) == 0u) { if (xb_ld(&(bar)[XB_TMO])) break; if (_sp > XB_SPIN_CAP) { atomicAdd(&(bar)[XB_TMO], 1u); break; } } } } while (0)
; DI void xcd_barrier(const XcdBarrier& b) {
;     ...
;     const unsigned gen = old / nloc;
;     if (old + 1u == (gen + 1u) * nloc) {
;       __builtin_amdgcn_fence(__ATOMIC_RELEASE, "agent");
;       asm volatile("s_waitcnt vmcnt(0)" ::: "memory");
;       const unsigned og = xb_add(&bar[XB_TOP], 1u);
;       const unsigned tg = og / nx;
;       if (og + 1u == (tg + 1u) * nx) xb_add(&bar[XB_TOPGEN], 1u);
;       else XB_SPIN(xb_ld(&bar[XB_TOPGEN]) == tg, bar);
;       __builtin_amdgcn_fence(__ATOMIC_ACQUIRE, "agent");
;       xb_add(&bar[XB_XGEN(b.x)], 1u);
;       asm volatile("s_waitcnt vmcnt(0)" ::: "memory");
;     } else {
;       XB_SPIN(xb_ld(&bar[XB_XGEN(b.x)]) == gen, bar);
;       __builtin_amdgcn_fence(__ATOMIC_ACQUIRE, "agent");
;       asm volatile("s_waitcnt vmcnt(0)" ::: "memory");
.LBB0_53:
	s_or_b64 exec, exec, s[8:9]
	v_cvt_f32_u32_e32 v4, v2
	s_waitcnt vmcnt(0)
	v_readfirstlane_b32 s2, v3
	v_sub_u32_e32 v3, 0, v2
	v_rcp_iflag_f32_e32 v4, v4
	v_add_u32_e32 v5, s2, v1
	v_mul_f32_e32 v4, 0x4f7ffffe, v4
	v_cvt_u32_f32_e32 v4, v4
	v_mul_lo_u32 v1, v3, v4
	v_mul_hi_u32 v1, v4, v1
	v_add_u32_e32 v1, v4, v1
	v_mul_hi_u32 v1, v5, v1
	v_mul_lo_u32 v3, v1, v2
	v_sub_u32_e32 v3, v5, v3
	v_add_u32_e32 v4, 1, v1
	v_cmp_ge_u32_e32 vcc, v3, v2
	s_nop 1
	v_cndmask_b32_e32 v1, v1, v4, vcc
	v_sub_u32_e32 v4, v3, v2
	v_cndmask_b32_e32 v3, v3, v4, vcc
	v_add_u32_e32 v4, 1, v1
	v_cmp_ge_u32_e32 vcc, v3, v2
	v_add_u32_e32 v3, 1, v5
	s_nop 0
	v_cndmask_b32_e32 v1, v1, v4, vcc
	v_mul_lo_u32 v4, v2, v1
	v_add_u32_e32 v2, v4, v2
	v_cmp_ne_u32_e32 vcc, v3, v2
	s_and_saveexec_b64 s[2:3], vcc
	s_xor_b64 s[6:7], exec, s[2:3]
	s_cbranch_execz .LBB0_67
	s_waitcnt lgkmcnt(0)
	buffer_inv sc1
	v_mov_b32_e32 v0, 0x4100
	global_load_dword v0, v0, s[84:85] offset:1024 sc1
	s_add_u32 s12, s84, 0x4500
	s_addc_u32 s13, s85, 0
	s_waitcnt vmcnt(0)
	v_cmp_eq_u32_e32 vcc, v0, v1
	s_and_saveexec_b64 s[8:9], vcc
	s_cbranch_execz .LBB0_66
	s_add_u32 s10, s84, 0x1200
	s_addc_u32 s11, s85, 0
	s_mov_b32 s2, 1
	s_mov_b64 s[14:15], 0
	v_mov_b32_e32 v0, 0
	s_branch .LBB0_57

; DI unsigned xb_ld(unsigned* p)              { return __hip_atomic_load(p, __ATOMIC_RELAXED, __HIP_MEMORY_SCOPE_AGENT); }
; DI unsigned xb_add(unsigned* p, unsigned v) { return __hip_atomic_fetch_add(p, v, __ATOMIC_RELAXED, __HIP_MEMORY_SCOPE_AGENT); }
; #define XB_SPIN(cond, bar) do { unsigned _sp = 0; while (cond) { __builtin_amdgcn_s_sleep(1); \
;     if ((++_sp & 255u) == 0u) { if (xb_ld(&(bar)[XB_TMO])) break; if (_sp > XB_SPIN_CAP) { atomicAdd(&(bar)[XB_TMO], 1u); break; } } } } while (0)
; DI void xcd_barrier(const XcdBarrier& b) {
;     ...
;     if (old + 1u == (gen + 1u) * nloc) {
;       __builtin_amdgcn_fence(__ATOMIC_RELEASE, "agent");
;       asm volatile("s_waitcnt vmcnt(0)" ::: "memory");
;       const unsigned og = xb_add(&bar[XB_TOP], 1u);
;       const unsigned tg = og / nx;
;       if (og + 1u == (tg + 1u) * nx) xb_add(&bar[XB_TOPGEN], 1u);
;       else XB_SPIN(xb_ld(&bar[XB_TOPGEN]) == tg, bar);
;       __builtin_amdgcn_fence(__ATOMIC_ACQUIRE, "agent");
;       xb_add(&bar[XB_XGEN(b.x)], 1u);
.LBB0_66:
	s_or_b64 exec, exec, s[8:9]
	s_waitcnt vmcnt(0)
	s_waitcnt vmcnt(0)
.LBB0_67:
	s_andn2_saveexec_b64 s[2:3], s[6:7]
	s_cbranch_execz .LBB0_87
	s_mov_b64 s[6:7], exec
	buffer_wbl2 sc1
	s_waitcnt lgkmcnt(0)
	s_waitcnt vmcnt(0)
	v_mbcnt_lo_u32_b32 v1, s6, 0
	v_mbcnt_hi_u32_b32 v1, s7, v1
	v_cmp_eq_u32_e32 vcc, 0, v1
	s_and_saveexec_b64 s[8:9], vcc
	s_cbranch_execz .LBB0_70
	s_bcnt1_i32_b64 s2, s[6:7]
	v_mov_b32_e32 v2, 0x4000
	v_mov_b32_e32 v3, s2
	global_atomic_add v2, v2, v3, s[84:85] offset:1024 sc0
	buffer_inv sc1

; DI unsigned xb_ld(unsigned* p)              { return __hip_atomic_load(p, __ATOMIC_RELAXED, __HIP_MEMORY_SCOPE_AGENT); }
; DI unsigned xb_add(unsigned* p, unsigned v) { return __hip_atomic_fetch_add(p, v, __ATOMIC_RELAXED, __HIP_MEMORY_SCOPE_AGENT); }
; #define XB_SPIN(cond, bar) do { unsigned _sp = 0; while (cond) { __builtin_amdgcn_s_sleep(1); \
;     if ((++_sp & 255u) == 0u) { if (xb_ld(&(bar)[XB_TMO])) break; if (_sp > XB_SPIN_CAP) { atomicAdd(&(bar)[XB_TMO], 1u); break; } } } } while (0)
; DI void xcd_barrier(const XcdBarrier& b) {
;     ...
;       else XB_SPIN(xb_ld(&bar[XB_TOPGEN]) == tg, bar);
;       __builtin_amdgcn_fence(__ATOMIC_ACQUIRE, "agent");
;       xb_add(&bar[XB_XGEN(b.x)], 1u);
.LBB0_84:
	s_or_b64 exec, exec, s[6:7]
	s_mov_b64 s[6:7], exec
	v_mbcnt_lo_u32_b32 v0, s6, 0
	v_mbcnt_hi_u32_b32 v0, s7, v0
	v_cmp_eq_u32_e32 vcc, 0, v0
	s_waitcnt vmcnt(0)
	s_and_saveexec_b64 s[8:9], vcc
	s_cbranch_execz .LBB0_86
	s_bcnt1_i32_b64 s2, s[6:7]
	v_mov_b32_e32 v0, 0x2000
	v_mov_b32_e32 v1, s2
	global_atomic_add v0, v1, s[4:5] offset:1024

; DI unsigned xb_ld(unsigned* p)              { return __hip_atomic_load(p, __ATOMIC_RELAXED, __HIP_MEMORY_SCOPE_AGENT); }
; DI unsigned xb_add(unsigned* p, unsigned v) { return __hip_atomic_fetch_add(p, v, __ATOMIC_RELAXED, __HIP_MEMORY_SCOPE_AGENT); }
; #define XB_SPIN(cond, bar) do { unsigned _sp = 0; while (cond) { __builtin_amdgcn_s_sleep(1); \
;     if ((++_sp & 255u) == 0u) { if (xb_ld(&(bar)[XB_TMO])) break; if (_sp > XB_SPIN_CAP) { atomicAdd(&(bar)[XB_TMO], 1u); break; } } } } while (0)
; DI void xcd_barrier(const XcdBarrier& b) {
;     ...
;     const unsigned gen = old / nloc;
;     if (old + 1u == (gen + 1u) * nloc) {
;       __builtin_amdgcn_fence(__ATOMIC_RELEASE, "agent");
;       asm volatile("s_waitcnt vmcnt(0)" ::: "memory");
;       const unsigned og = xb_add(&bar[XB_TOP], 1u);
;       const unsigned tg = og / nx;
;       if (og + 1u == (tg + 1u) * nx) xb_add(&bar[XB_TOPGEN], 1u);
;       else XB_SPIN(xb_ld(&bar[XB_TOPGEN]) == tg, bar);
;       __builtin_amdgcn_fence(__ATOMIC_ACQUIRE, "agent");
;       xb_add(&bar[XB_XGEN(b.x)], 1u);
;       asm volatile("s_waitcnt vmcnt(0)" ::: "memory");
;     } else {
;       XB_SPIN(xb_ld(&bar[XB_XGEN(b.x)]) == gen, bar);
;       __builtin_amdgcn_fence(__ATOMIC_ACQUIRE, "agent");
;       asm volatile("s_waitcnt vmcnt(0)" ::: "memory");
.LBB0_1173:
	s_or_b64 exec, exec, s[12:13]
	v_cvt_f32_u32_e32 v4, v2
	s_waitcnt vmcnt(0)
	v_readfirstlane_b32 s2, v3
	v_sub_u32_e32 v3, 0, v2
	v_rcp_iflag_f32_e32 v4, v4
	v_add_u32_e32 v5, s2, v1
	v_mul_f32_e32 v4, 0x4f7ffffe, v4
	v_cvt_u32_f32_e32 v4, v4
	v_mul_lo_u32 v1, v3, v4
	v_mul_hi_u32 v1, v4, v1
	v_add_u32_e32 v1, v4, v1
	v_mul_hi_u32 v1, v5, v1
	v_mul_lo_u32 v3, v1, v2
	v_sub_u32_e32 v3, v5, v3
	v_add_u32_e32 v4, 1, v1
	v_cmp_ge_u32_e32 vcc, v3, v2
	s_nop 1
	v_cndmask_b32_e32 v1, v1, v4, vcc
	v_sub_u32_e32 v4, v3, v2
	v_cndmask_b32_e32 v3, v3, v4, vcc
	v_add_u32_e32 v4, 1, v1
	v_cmp_ge_u32_e32 vcc, v3, v2
	v_add_u32_e32 v3, 1, v5
	s_nop 0
	v_cndmask_b32_e32 v1, v1, v4, vcc
	v_mul_lo_u32 v4, v2, v1
	v_add_u32_e32 v2, v4, v2
	v_cmp_ne_u32_e32 vcc, v3, v2
	s_and_saveexec_b64 s[2:3], vcc
	s_xor_b64 s[10:11], exec, s[2:3]
	s_cbranch_execz .LBB0_1187
	s_waitcnt lgkmcnt(0)
	buffer_inv sc1
	v_mov_b32_e32 v0, 0x4100
	global_load_dword v0, v0, s[84:85] offset:1024 sc1
	s_add_u32 s16, s84, 0x4500
	s_addc_u32 s17, s85, 0
	s_waitcnt vmcnt(0)
	v_cmp_eq_u32_e32 vcc, v0, v1
	s_and_saveexec_b64 s[12:13], vcc
	s_cbranch_execz .LBB0_1186
	s_add_u32 s14, s84, 0x1200
	s_addc_u32 s15, s85, 0
	s_mov_b32 s2, 1
	s_mov_b64 s[24:25], 0
	v_mov_b32_e32 v0, 0
	s_branch .LBB0_1177

; DI unsigned xb_ld(unsigned* p)              { return __hip_atomic_load(p, __ATOMIC_RELAXED, __HIP_MEMORY_SCOPE_AGENT); }
; DI unsigned xb_add(unsigned* p, unsigned v) { return __hip_atomic_fetch_add(p, v, __ATOMIC_RELAXED, __HIP_MEMORY_SCOPE_AGENT); }
; #define XB_SPIN(cond, bar) do { unsigned _sp = 0; while (cond) { __builtin_amdgcn_s_sleep(1); \
;     if ((++_sp & 255u) == 0u) { if (xb_ld(&(bar)[XB_TMO])) break; if (_sp > XB_SPIN_CAP) { atomicAdd(&(bar)[XB_TMO], 1u); break; } } } } while (0)
; DI void xcd_barrier(const XcdBarrier& b) {
;     ...
;     if (old + 1u == (gen + 1u) * nloc) {
;       __builtin_amdgcn_fence(__ATOMIC_RELEASE, "agent");
;       asm volatile("s_waitcnt vmcnt(0)" ::: "memory");
;       const unsigned og = xb_add(&bar[XB_TOP], 1u);
;       const unsigned tg = og / nx;
;       if (og + 1u == (tg + 1u) * nx) xb_add(&bar[XB_TOPGEN], 1u);
;       else XB_SPIN(xb_ld(&bar[XB_TOPGEN]) == tg, bar);
;       __builtin_amdgcn_fence(__ATOMIC_ACQUIRE, "agent");
;       xb_add(&bar[XB_XGEN(b.x)], 1u);
.LBB0_1186:
	s_or_b64 exec, exec, s[12:13]
	s_waitcnt vmcnt(0)
	s_waitcnt vmcnt(0)
.LBB0_1187:
	s_andn2_saveexec_b64 s[2:3], s[10:11]
	s_cbranch_execz .LBB0_1207
	s_mov_b64 s[10:11], exec
	buffer_wbl2 sc1
	s_waitcnt lgkmcnt(0)
	s_waitcnt vmcnt(0)
	v_mbcnt_lo_u32_b32 v1, s10, 0
	v_mbcnt_hi_u32_b32 v1, s11, v1
	v_cmp_eq_u32_e32 vcc, 0, v1
	s_and_saveexec_b64 s[12:13], vcc
	s_cbranch_execz .LBB0_1190
	s_bcnt1_i32_b64 s2, s[10:11]
	v_mov_b32_e32 v2, 0x4000
	v_mov_b32_e32 v3, s2
	global_atomic_add v2, v2, v3, s[84:85] offset:1024 sc0
	buffer_inv sc1

; DI unsigned xb_ld(unsigned* p)              { return __hip_atomic_load(p, __ATOMIC_RELAXED, __HIP_MEMORY_SCOPE_AGENT); }
; DI unsigned xb_add(unsigned* p, unsigned v) { return __hip_atomic_fetch_add(p, v, __ATOMIC_RELAXED, __HIP_MEMORY_SCOPE_AGENT); }
; #define XB_SPIN(cond, bar) do { unsigned _sp = 0; while (cond) { __builtin_amdgcn_s_sleep(1); \
;     if ((++_sp & 255u) == 0u) { if (xb_ld(&(bar)[XB_TMO])) break; if (_sp > XB_SPIN_CAP) { atomicAdd(&(bar)[XB_TMO], 1u); break; } } } } while (0)
; DI void xcd_barrier(const XcdBarrier& b) {
;     ...
;       else XB_SPIN(xb_ld(&bar[XB_TOPGEN]) == tg, bar);
;       __builtin_amdgcn_fence(__ATOMIC_ACQUIRE, "agent");
;       xb_add(&bar[XB_XGEN(b.x)], 1u);
.LBB0_1204:
	s_or_b64 exec, exec, s[10:11]
	s_mov_b64 s[10:11], exec
	v_mbcnt_lo_u32_b32 v0, s10, 0
	v_mbcnt_hi_u32_b32 v0, s11, v0
	v_cmp_eq_u32_e32 vcc, 0, v0
	s_waitcnt vmcnt(0)
	s_and_saveexec_b64 s[12:13], vcc
	s_cbranch_execz .LBB0_1206
	s_bcnt1_i32_b64 s2, s[10:11]
	v_mov_b32_e32 v0, 0x2000
	v_mov_b32_e32 v1, s2
	global_atomic_add v0, v1, s[8:9] offset:1024

; DI unsigned xb_ld(unsigned* p)              { return __hip_atomic_load(p, __ATOMIC_RELAXED, __HIP_MEMORY_SCOPE_AGENT); }
; DI unsigned xb_add(unsigned* p, unsigned v) { return __hip_atomic_fetch_add(p, v, __ATOMIC_RELAXED, __HIP_MEMORY_SCOPE_AGENT); }
; #define XB_SPIN(cond, bar) do { unsigned _sp = 0; while (cond) { __builtin_amdgcn_s_sleep(1); \
;     if ((++_sp & 255u) == 0u) { if (xb_ld(&(bar)[XB_TMO])) break; if (_sp > XB_SPIN_CAP) { atomicAdd(&(bar)[XB_TMO], 1u); break; } } } } while (0)
; DI void xcd_barrier(const XcdBarrier& b) {
;     ...
;     const unsigned gen = old / nloc;
;     if (old + 1u == (gen + 1u) * nloc) {
;       __builtin_amdgcn_fence(__ATOMIC_RELEASE, "agent");
;       asm volatile("s_waitcnt vmcnt(0)" ::: "memory");
;       const unsigned og = xb_add(&bar[XB_TOP], 1u);
;       const unsigned tg = og / nx;
;       if (og + 1u == (tg + 1u) * nx) xb_add(&bar[XB_TOPGEN], 1u);
;       else XB_SPIN(xb_ld(&bar[XB_TOPGEN]) == tg, bar);
;       __builtin_amdgcn_fence(__ATOMIC_ACQUIRE, "agent");
;       xb_add(&bar[XB_XGEN(b.x)], 1u);
;       asm volatile("s_waitcnt vmcnt(0)" ::: "memory");
;     } else {
;       XB_SPIN(xb_ld(&bar[XB_XGEN(b.x)]) == gen, bar);
;       __builtin_amdgcn_fence(__ATOMIC_ACQUIRE, "agent");
;       asm volatile("s_waitcnt vmcnt(0)" ::: "memory");
.LBB0_1300:
	s_or_b64 exec, exec, s[10:11]
	v_cvt_f32_u32_e32 v4, v2
	s_waitcnt vmcnt(0)
	v_readfirstlane_b32 s2, v3
	v_sub_u32_e32 v3, 0, v2
	v_rcp_iflag_f32_e32 v4, v4
	v_add_u32_e32 v5, s2, v1
	v_mul_f32_e32 v4, 0x4f7ffffe, v4
	v_cvt_u32_f32_e32 v4, v4
	v_mul_lo_u32 v1, v3, v4
	v_mul_hi_u32 v1, v4, v1
	v_add_u32_e32 v1, v4, v1
	v_mul_hi_u32 v1, v5, v1
	v_mul_lo_u32 v3, v1, v2
	v_sub_u32_e32 v3, v5, v3
	v_add_u32_e32 v4, 1, v1
	v_cmp_ge_u32_e32 vcc, v3, v2
	s_nop 1
	v_cndmask_b32_e32 v1, v1, v4, vcc
	v_sub_u32_e32 v4, v3, v2
	v_cndmask_b32_e32 v3, v3, v4, vcc
	v_add_u32_e32 v4, 1, v1
	v_cmp_ge_u32_e32 vcc, v3, v2
	v_add_u32_e32 v3, 1, v5
	s_nop 0
	v_cndmask_b32_e32 v1, v1, v4, vcc
	v_mul_lo_u32 v4, v2, v1
	v_add_u32_e32 v2, v4, v2
	v_cmp_ne_u32_e32 vcc, v3, v2
	s_and_saveexec_b64 s[2:3], vcc
	s_xor_b64 s[8:9], exec, s[2:3]
	s_cbranch_execz .LBB0_1314
	s_waitcnt lgkmcnt(0)
	buffer_inv sc1
	v_mov_b32_e32 v0, 0x4100
	global_load_dword v0, v0, s[84:85] offset:1024 sc1
	s_add_u32 s14, s84, 0x4500
	s_addc_u32 s15, s85, 0
	s_waitcnt vmcnt(0)
	v_cmp_eq_u32_e32 vcc, v0, v1
	s_and_saveexec_b64 s[10:11], vcc
	s_cbranch_execz .LBB0_1313
	s_add_u32 s12, s84, 0x1200
	s_addc_u32 s13, s85, 0
	s_mov_b32 s2, 1
	s_mov_b64 s[16:17], 0
	v_mov_b32_e32 v0, 0
	s_branch .LBB0_1304

; DI unsigned xb_ld(unsigned* p)              { return __hip_atomic_load(p, __ATOMIC_RELAXED, __HIP_MEMORY_SCOPE_AGENT); }
; DI unsigned xb_add(unsigned* p, unsigned v) { return __hip_atomic_fetch_add(p, v, __ATOMIC_RELAXED, __HIP_MEMORY_SCOPE_AGENT); }
; #define XB_SPIN(cond, bar) do { unsigned _sp = 0; while (cond) { __builtin_amdgcn_s_sleep(1); \
;     if ((++_sp & 255u) == 0u) { if (xb_ld(&(bar)[XB_TMO])) break; if (_sp > XB_SPIN_CAP) { atomicAdd(&(bar)[XB_TMO], 1u); break; } } } } while (0)
; DI void xcd_barrier(const XcdBarrier& b) {
;     ...
;     if (old + 1u == (gen + 1u) * nloc) {
;       __builtin_amdgcn_fence(__ATOMIC_RELEASE, "agent");
;       asm volatile("s_waitcnt vmcnt(0)" ::: "memory");
;       const unsigned og = xb_add(&bar[XB_TOP], 1u);
;       const unsigned tg = og / nx;
;       if (og + 1u == (tg + 1u) * nx) xb_add(&bar[XB_TOPGEN], 1u);
;       else XB_SPIN(xb_ld(&bar[XB_TOPGEN]) == tg, bar);
;       __builtin_amdgcn_fence(__ATOMIC_ACQUIRE, "agent");
;       xb_add(&bar[XB_XGEN(b.x)], 1u);
.LBB0_1313:
	s_or_b64 exec, exec, s[10:11]
	s_waitcnt vmcnt(0)
	s_waitcnt vmcnt(0)
.LBB0_1314:
	s_andn2_saveexec_b64 s[2:3], s[8:9]
	s_cbranch_execz .LBB0_1334
	s_mov_b64 s[8:9], exec
	buffer_wbl2 sc1
	s_waitcnt lgkmcnt(0)
	s_waitcnt vmcnt(0)
	v_mbcnt_lo_u32_b32 v1, s8, 0
	v_mbcnt_hi_u32_b32 v1, s9, v1
	v_cmp_eq_u32_e32 vcc, 0, v1
	s_and_saveexec_b64 s[10:11], vcc
	s_cbranch_execz .LBB0_1317
	s_bcnt1_i32_b64 s2, s[8:9]
	v_mov_b32_e32 v2, 0x4000
	v_mov_b32_e32 v3, s2
	global_atomic_add v2, v2, v3, s[84:85] offset:1024 sc0
	buffer_inv sc1

; DI unsigned xb_ld(unsigned* p)              { return __hip_atomic_load(p, __ATOMIC_RELAXED, __HIP_MEMORY_SCOPE_AGENT); }
; DI unsigned xb_add(unsigned* p, unsigned v) { return __hip_atomic_fetch_add(p, v, __ATOMIC_RELAXED, __HIP_MEMORY_SCOPE_AGENT); }
; #define XB_SPIN(cond, bar) do { unsigned _sp = 0; while (cond) { __builtin_amdgcn_s_sleep(1); \
;     if ((++_sp & 255u) == 0u) { if (xb_ld(&(bar)[XB_TMO])) break; if (_sp > XB_SPIN_CAP) { atomicAdd(&(bar)[XB_TMO], 1u); break; } } } } while (0)
; DI void xcd_barrier(const XcdBarrier& b) {
;     ...
;       else XB_SPIN(xb_ld(&bar[XB_TOPGEN]) == tg, bar);
;       __builtin_amdgcn_fence(__ATOMIC_ACQUIRE, "agent");
;       xb_add(&bar[XB_XGEN(b.x)], 1u);
.LBB0_1331:
	s_or_b64 exec, exec, s[8:9]
	s_mov_b64 s[8:9], exec
	v_mbcnt_lo_u32_b32 v0, s8, 0
	v_mbcnt_hi_u32_b32 v0, s9, v0
	v_cmp_eq_u32_e32 vcc, 0, v0
	s_waitcnt vmcnt(0)
	s_and_saveexec_b64 s[10:11], vcc
	s_cbranch_execz .LBB0_1333
	s_bcnt1_i32_b64 s2, s[8:9]
	v_mov_b32_e32 v0, 0x2000
	v_mov_b32_e32 v1, s2
	global_atomic_add v0, v1, s[6:7] offset:1024

; DI unsigned xb_ld(unsigned* p)              { return __hip_atomic_load(p, __ATOMIC_RELAXED, __HIP_MEMORY_SCOPE_AGENT); }
; DI unsigned xb_add(unsigned* p, unsigned v) { return __hip_atomic_fetch_add(p, v, __ATOMIC_RELAXED, __HIP_MEMORY_SCOPE_AGENT); }
; #define XB_SPIN(cond, bar) do { unsigned _sp = 0; while (cond) { __builtin_amdgcn_s_sleep(1); \
;     if ((++_sp & 255u) == 0u) { if (xb_ld(&(bar)[XB_TMO])) break; if (_sp > XB_SPIN_CAP) { atomicAdd(&(bar)[XB_TMO], 1u); break; } } } } while (0)
; DI void xcd_barrier(const XcdBarrier& b) {
;     ...
;     const unsigned gen = old / nloc;
;     if (old + 1u == (gen + 1u) * nloc) {
;       __builtin_amdgcn_fence(__ATOMIC_RELEASE, "agent");
;       asm volatile("s_waitcnt vmcnt(0)" ::: "memory");
;       const unsigned og = xb_add(&bar[XB_TOP], 1u);
;       const unsigned tg = og / nx;
;       if (og + 1u == (tg + 1u) * nx) xb_add(&bar[XB_TOPGEN], 1u);
;       else XB_SPIN(xb_ld(&bar[XB_TOPGEN]) == tg, bar);
;       __builtin_amdgcn_fence(__ATOMIC_ACQUIRE, "agent");
;       xb_add(&bar[XB_XGEN(b.x)], 1u);
;       asm volatile("s_waitcnt vmcnt(0)" ::: "memory");
;     } else {
;       XB_SPIN(xb_ld(&bar[XB_XGEN(b.x)]) == gen, bar);
;       __builtin_amdgcn_fence(__ATOMIC_ACQUIRE, "agent");
;       asm volatile("s_waitcnt vmcnt(0)" ::: "memory");
.LBB0_1771:
	s_or_b64 exec, exec, s[6:7]
	v_cvt_f32_u32_e32 v4, v2
	s_waitcnt vmcnt(0)
	v_readfirstlane_b32 s4, v3
	v_sub_u32_e32 v3, 0, v2
	v_rcp_iflag_f32_e32 v4, v4
	v_add_u32_e32 v5, s4, v1
	v_mul_f32_e32 v4, 0x4f7ffffe, v4
	v_cvt_u32_f32_e32 v4, v4
	v_mul_lo_u32 v1, v3, v4
	v_mul_hi_u32 v1, v4, v1
	v_add_u32_e32 v1, v4, v1
	v_mul_hi_u32 v1, v5, v1
	v_mul_lo_u32 v3, v1, v2
	v_sub_u32_e32 v3, v5, v3
	v_add_u32_e32 v4, 1, v1
	v_cmp_ge_u32_e32 vcc, v3, v2
	s_nop 1
	v_cndmask_b32_e32 v1, v1, v4, vcc
	v_sub_u32_e32 v4, v3, v2
	v_cndmask_b32_e32 v3, v3, v4, vcc
	v_add_u32_e32 v4, 1, v1
	v_cmp_ge_u32_e32 vcc, v3, v2
	v_add_u32_e32 v3, 1, v5
	s_nop 0
	v_cndmask_b32_e32 v1, v1, v4, vcc
	v_mul_lo_u32 v4, v2, v1
	v_add_u32_e32 v2, v4, v2
	v_cmp_ne_u32_e32 vcc, v3, v2
	s_and_saveexec_b64 s[4:5], vcc
	s_xor_b64 s[4:5], exec, s[4:5]
	s_cbranch_execz .LBB0_1785
	s_waitcnt lgkmcnt(0)
	buffer_inv sc1
	v_mov_b32_e32 v0, 0x4100
	global_load_dword v0, v0, s[84:85] offset:1024 sc1
	s_add_u32 s10, s84, 0x4500
	s_addc_u32 s11, s85, 0
	s_waitcnt vmcnt(0)
	v_cmp_eq_u32_e32 vcc, v0, v1
	s_and_saveexec_b64 s[6:7], vcc
	s_cbranch_execz .LBB0_1784
	s_add_u32 s8, s84, 0x1200
	s_addc_u32 s9, s85, 0
	s_mov_b32 s26, 1
	s_mov_b64 s[12:13], 0
	v_mov_b32_e32 v0, 0
	s_branch .LBB0_1775

; DI unsigned xb_ld(unsigned* p)              { return __hip_atomic_load(p, __ATOMIC_RELAXED, __HIP_MEMORY_SCOPE_AGENT); }
; DI unsigned xb_add(unsigned* p, unsigned v) { return __hip_atomic_fetch_add(p, v, __ATOMIC_RELAXED, __HIP_MEMORY_SCOPE_AGENT); }
; #define XB_SPIN(cond, bar) do { unsigned _sp = 0; while (cond) { __builtin_amdgcn_s_sleep(1); \
;     if ((++_sp & 255u) == 0u) { if (xb_ld(&(bar)[XB_TMO])) break; if (_sp > XB_SPIN_CAP) { atomicAdd(&(bar)[XB_TMO], 1u); break; } } } } while (0)
; DI void xcd_barrier(const XcdBarrier& b) {
;     ...
;     if (old + 1u == (gen + 1u) * nloc) {
;       __builtin_amdgcn_fence(__ATOMIC_RELEASE, "agent");
;       asm volatile("s_waitcnt vmcnt(0)" ::: "memory");
;       const unsigned og = xb_add(&bar[XB_TOP], 1u);
;       const unsigned tg = og / nx;
;       if (og + 1u == (tg + 1u) * nx) xb_add(&bar[XB_TOPGEN], 1u);
;       else XB_SPIN(xb_ld(&bar[XB_TOPGEN]) == tg, bar);
;       __builtin_amdgcn_fence(__ATOMIC_ACQUIRE, "agent");
;       xb_add(&bar[XB_XGEN(b.x)], 1u);
.LBB0_1784:
	s_or_b64 exec, exec, s[6:7]
	s_waitcnt vmcnt(0)
	s_waitcnt vmcnt(0)
.LBB0_1785:
	s_andn2_saveexec_b64 s[4:5], s[4:5]
	s_cbranch_execz .LBB0_1805
	s_mov_b64 s[4:5], exec
	buffer_wbl2 sc1
	s_waitcnt lgkmcnt(0)
	s_waitcnt vmcnt(0)
	v_mbcnt_lo_u32_b32 v1, s4, 0
	v_mbcnt_hi_u32_b32 v1, s5, v1
	v_cmp_eq_u32_e32 vcc, 0, v1
	s_and_saveexec_b64 s[6:7], vcc
	s_cbranch_execz .LBB0_1788
	s_bcnt1_i32_b64 s4, s[4:5]
	v_mov_b32_e32 v2, 0x4000
	v_mov_b32_e32 v3, s4
	global_atomic_add v2, v2, v3, s[84:85] offset:1024 sc0
	buffer_inv sc1

; DI unsigned xb_ld(unsigned* p)              { return __hip_atomic_load(p, __ATOMIC_RELAXED, __HIP_MEMORY_SCOPE_AGENT); }
; DI unsigned xb_add(unsigned* p, unsigned v) { return __hip_atomic_fetch_add(p, v, __ATOMIC_RELAXED, __HIP_MEMORY_SCOPE_AGENT); }
; #define XB_SPIN(cond, bar) do { unsigned _sp = 0; while (cond) { __builtin_amdgcn_s_sleep(1); \
;     if ((++_sp & 255u) == 0u) { if (xb_ld(&(bar)[XB_TMO])) break; if (_sp > XB_SPIN_CAP) { atomicAdd(&(bar)[XB_TMO], 1u); break; } } } } while (0)
; DI void xcd_barrier(const XcdBarrier& b) {
;     ...
;       else XB_SPIN(xb_ld(&bar[XB_TOPGEN]) == tg, bar);
;       __builtin_amdgcn_fence(__ATOMIC_ACQUIRE, "agent");
;       xb_add(&bar[XB_XGEN(b.x)], 1u);
.LBB0_1802:
	s_or_b64 exec, exec, s[4:5]
	s_mov_b64 s[4:5], exec
	v_mbcnt_lo_u32_b32 v0, s4, 0
	v_mbcnt_hi_u32_b32 v0, s5, v0
	v_cmp_eq_u32_e32 vcc, 0, v0
	s_waitcnt vmcnt(0)
	s_and_saveexec_b64 s[6:7], vcc
	s_cbranch_execz .LBB0_1804
	s_bcnt1_i32_b64 s4, s[4:5]
	v_mov_b32_e32 v0, 0x2000
	v_mov_b32_e32 v1, s4
	global_atomic_add v0, v1, s[2:3] offset:1024

; DI unsigned xb_ld(unsigned* p)              { return __hip_atomic_load(p, __ATOMIC_RELAXED, __HIP_MEMORY_SCOPE_AGENT); }
; DI unsigned xb_add(unsigned* p, unsigned v) { return __hip_atomic_fetch_add(p, v, __ATOMIC_RELAXED, __HIP_MEMORY_SCOPE_AGENT); }
; #define XB_SPIN(cond, bar) do { unsigned _sp = 0; while (cond) { __builtin_amdgcn_s_sleep(1); \
;     if ((++_sp & 255u) == 0u) { if (xb_ld(&(bar)[XB_TMO])) break; if (_sp > XB_SPIN_CAP) { atomicAdd(&(bar)[XB_TMO], 1u); break; } } } } while (0)
; DI void xcd_barrier(const XcdBarrier& b) {
;     ...
;     const unsigned gen = old / nloc;
;     if (old + 1u == (gen + 1u) * nloc) {
;       __builtin_amdgcn_fence(__ATOMIC_RELEASE, "agent");
;       asm volatile("s_waitcnt vmcnt(0)" ::: "memory");
;       const unsigned og = xb_add(&bar[XB_TOP], 1u);
;       const unsigned tg = og / nx;
;       if (og + 1u == (tg + 1u) * nx) xb_add(&bar[XB_TOPGEN], 1u);
;       else XB_SPIN(xb_ld(&bar[XB_TOPGEN]) == tg, bar);
;       __builtin_amdgcn_fence(__ATOMIC_ACQUIRE, "agent");
;       xb_add(&bar[XB_XGEN(b.x)], 1u);
;       asm volatile("s_waitcnt vmcnt(0)" ::: "memory");
;     } else {
;       XB_SPIN(xb_ld(&bar[XB_XGEN(b.x)]) == gen, bar);
;       __builtin_amdgcn_fence(__ATOMIC_ACQUIRE, "agent");
;       asm volatile("s_waitcnt vmcnt(0)" ::: "memory");
.LBB0_1907:
	s_or_b64 exec, exec, s[6:7]
	v_cvt_f32_u32_e32 v4, v2
	s_waitcnt vmcnt(0)
	v_readfirstlane_b32 s4, v3
	v_sub_u32_e32 v3, 0, v2
	v_rcp_iflag_f32_e32 v4, v4
	v_add_u32_e32 v5, s4, v1
	v_mul_f32_e32 v4, 0x4f7ffffe, v4
	v_cvt_u32_f32_e32 v4, v4
	v_mul_lo_u32 v1, v3, v4
	v_mul_hi_u32 v1, v4, v1
	v_add_u32_e32 v1, v4, v1
	v_mul_hi_u32 v1, v5, v1
	v_mul_lo_u32 v3, v1, v2
	v_sub_u32_e32 v3, v5, v3
	v_add_u32_e32 v4, 1, v1
	v_cmp_ge_u32_e32 vcc, v3, v2
	s_nop 1
	v_cndmask_b32_e32 v1, v1, v4, vcc
	v_sub_u32_e32 v4, v3, v2
	v_cndmask_b32_e32 v3, v3, v4, vcc
	v_add_u32_e32 v4, 1, v1
	v_cmp_ge_u32_e32 vcc, v3, v2
	v_add_u32_e32 v3, 1, v5
	s_nop 0
	v_cndmask_b32_e32 v1, v1, v4, vcc
	v_mul_lo_u32 v4, v2, v1
	v_add_u32_e32 v2, v4, v2
	v_cmp_ne_u32_e32 vcc, v3, v2
	s_and_saveexec_b64 s[4:5], vcc
	s_xor_b64 s[4:5], exec, s[4:5]
	s_cbranch_execz .LBB0_1921
	s_waitcnt lgkmcnt(0)
	buffer_inv sc1
	v_mov_b32_e32 v0, 0x4100
	global_load_dword v0, v0, s[84:85] offset:1024 sc1
	s_add_u32 s10, s84, 0x4500
	s_addc_u32 s11, s85, 0
	s_waitcnt vmcnt(0)
	v_cmp_eq_u32_e32 vcc, v0, v1
	s_and_saveexec_b64 s[6:7], vcc
	s_cbranch_execz .LBB0_1920
	s_add_u32 s8, s84, 0x1200
	s_addc_u32 s9, s85, 0
	s_mov_b32 s22, 1
	s_mov_b64 s[12:13], 0
	v_mov_b32_e32 v0, 0
	s_branch .LBB0_1911
